# as previous plus w_out1, glu_w and w_in1 fp16 conversions moved from the prologue into the 64 converter workgroups beside the first GEMM
# baseline (speedup 1.0000x reference)
.LBB0_120:
	s_or_b64 exec, exec, s[0:1]
	s_cmp_eq_u32 s99, 0
	s_cbranch_scc0 .Lconv_ret_h0
	s_movk_i32 s0, 0xb00
	v_cmp_gt_i32_e32 vcc, s0, v69
	s_and_saveexec_b64 s[0:1], vcc
	s_cbranch_execz .LBB0_191
	v_lshlrev_b32_e32 v2, 2, v78
	v_mov_b32_e32 v3, 0
	v_lshl_add_u64 v[18:19], s[50:51], 0, v[2:3]
	v_mul_u32_u24_e32 v2, 0x84, v66
	s_mov_b64 s[8:9], 0x3ad00000
	v_add_u32_e32 v30, v79, v2
	v_lshl_add_u64 v[20:21], v[80:81], 0, s[8:9]
	s_lshl_b32 s12, s3, 7
	s_mov_b64 s[8:9], 0
	s_mov_b32 s13, 0x2e8ba2e9
	s_movk_i32 s14, 0xea00
	v_add_u32_e32 v31, 0x420, v30
	v_add_u32_e32 v32, 0x428, v30
	v_add_u32_e32 v33, 0x840, v30
	v_add_u32_e32 v34, 0x848, v30
	v_add_u32_e32 v35, 0xc60, v30
	v_add_u32_e32 v36, 0xc68, v30
	v_add_u32_e32 v37, 0x1080, v30
	v_add_u32_e32 v38, 0x1088, v30
	v_add_u32_e32 v39, 0x14a0, v30
	v_add_u32_e32 v40, 0x14a8, v30
	v_add_u32_e32 v41, 0x18c0, v30
	v_add_u32_e32 v42, 0x18c8, v30
	v_add_u32_e32 v43, 0x1ce0, v30
	v_add_u32_e32 v44, 0x1ce8, v30
	v_add_u32_e32 v45, 0x2100, v30
	v_add_u32_e32 v46, 0x2108, v30
	v_add_u32_e32 v47, 0x2520, v30
	v_add_u32_e32 v48, 0x2528, v30
	v_add_u32_e32 v49, 0x2940, v30
	v_add_u32_e32 v50, 0x2948, v30
	v_add_u32_e32 v51, 0x2d60, v30
	v_add_u32_e32 v52, 0x2d68, v30
	v_add_u32_e32 v53, 0x3180, v30
	v_add_u32_e32 v54, 0x3188, v30
	v_add_u32_e32 v55, 0x35a0, v30
	v_add_u32_e32 v56, 0x35a8, v30
	v_add_u32_e32 v57, 0x39c0, v30
	v_add_u32_e32 v58, 0x39c8, v30
	v_add_u32_e32 v59, 0x3de0, v30
	v_add_u32_e32 v60, 0x3de8, v30
	s_mov_b32 s15, 0xc3e00000
	v_mov_b32_e32 v61, 0x43e00000
	s_movk_i32 s16, 0x1600
	s_movk_i32 s17, 0xaff
	v_add_u32_e32 v62, 0x400, v75
	v_add_u32_e32 v63, 0x600, v75
	v_mov_b32_e32 v64, v69

.LBB0_400:
	s_cmp_lt_i32 s76, 2
	s_cselect_b64 s[6:7], -1, 0
	s_add_u32 s82, s58, 0x32100000
	s_addc_u32 s83, s59, 0
	s_and_b64 s[0:1], s[6:7], s[0:1]
	s_andn2_b64 vcc, exec, s[0:1]
	s_cbranch_vccnz .LBB0_417
	s_mov_b32 s101, s2
	s_cmpk_lt_i32 s96, 192
	s_cbranch_scc1 .Lh0_gemm
	s_sub_i32 s96, s96, 192
	s_movk_i32 s2, 64
	s_mov_b32 s98, 2
	s_mov_b32 s100, 5
	s_mov_b32 s99, 1
	v_readlane_b32 s6, v239, 34
	v_readlane_b32 s7, v239, 35
	s_nop 3
	s_sub_u32 s6, s6, 0x128
	s_subb_u32 s7, s7, 0
	s_load_dwordx2 s[82:83], s[6:7], 0xc8
	s_waitcnt lgkmcnt(0)
	s_branch .Lconv_entry
